# P7 router MFMA loop unrolled with W tiles of three k-iterations preloaded into spare registers and counted waits
# baseline (speedup 1.0000x reference)
.LBB0_1139:
	global_load_dword v240, v[92:93], off
	global_load_dwordx4 v[116:119], v[112:113], off offset:-256
	global_load_dwordx4 v[120:123], v[112:113], off offset:-192
	global_load_dwordx4 v[124:127], v[112:113], off offset:-128
	global_load_dwordx4 v[128:131], v[112:113], off offset:-64
	global_load_dwordx4 v[132:135], v[112:113], off
	global_load_dwordx4 v[136:139], v[112:113], off offset:64
	global_load_dwordx4 v[140:143], v[112:113], off offset:128
	global_load_dwordx4 v[144:147], v[112:113], off offset:192
	global_load_dwordx4 v[156:159], v[112:113], off offset:256
	global_load_dwordx4 v[160:163], v[112:113], off offset:320
	global_load_dwordx4 v[164:167], v[112:113], off offset:384
	global_load_dwordx4 v[168:171], v[112:113], off offset:448
	global_load_dwordx4 v[172:175], v[112:113], off offset:512
	global_load_dwordx4 v[176:179], v[112:113], off offset:576
	global_load_dwordx4 v[180:183], v[112:113], off offset:640
	global_load_dwordx4 v[184:187], v[112:113], off offset:704
	global_load_dwordx4 v[208:211], v[112:113], off offset:768
	global_load_dwordx4 v[212:215], v[112:113], off offset:832
	global_load_dwordx4 v[216:219], v[112:113], off offset:896
	global_load_dwordx4 v[220:223], v[112:113], off offset:960
	global_load_dwordx4 v[224:227], v[112:113], off offset:1024
	global_load_dwordx4 v[228:231], v[112:113], off offset:1088
	global_load_dwordx4 v[232:235], v[112:113], off offset:1152
	global_load_dwordx4 v[236:239], v[112:113], off offset:1216
	v_mov_b32_e32 v66, 0
	v_mov_b32_e32 v67, 0
	v_mov_b32_e32 v68, 0
	v_mov_b32_e32 v69, 0
	ds_read_b128 v[148:151], v1
	ds_read_b128 v[152:155], v1 offset:64
	s_waitcnt vmcnt(23) lgkmcnt(1)
	v_mfma_f32_16x16x32_bf16 v[66:69], v[148:151], v[116:119], v[66:69]
	ds_read_b128 v[188:191], v1 offset:128
	s_waitcnt vmcnt(22) lgkmcnt(1)
	v_mfma_f32_16x16x32_bf16 v[66:69], v[152:155], v[120:123], v[66:69]
	ds_read_b128 v[244:247], v1 offset:192
	s_waitcnt vmcnt(21) lgkmcnt(1)
	v_mfma_f32_16x16x32_bf16 v[66:69], v[188:191], v[124:127], v[66:69]
	ds_read_b128 v[148:151], v1 offset:256
	s_waitcnt vmcnt(20) lgkmcnt(1)
	v_mfma_f32_16x16x32_bf16 v[66:69], v[244:247], v[128:131], v[66:69]
	ds_read_b128 v[152:155], v1 offset:320
	s_waitcnt vmcnt(19) lgkmcnt(1)
	v_mfma_f32_16x16x32_bf16 v[66:69], v[148:151], v[132:135], v[66:69]
	ds_read_b128 v[188:191], v1 offset:384
	s_waitcnt vmcnt(18) lgkmcnt(1)
	v_mfma_f32_16x16x32_bf16 v[66:69], v[152:155], v[136:139], v[66:69]
	ds_read_b128 v[244:247], v1 offset:448
	s_waitcnt vmcnt(17) lgkmcnt(1)
	v_mfma_f32_16x16x32_bf16 v[66:69], v[188:191], v[140:143], v[66:69]
	s_waitcnt vmcnt(16) lgkmcnt(0)
	v_mfma_f32_16x16x32_bf16 v[66:69], v[244:247], v[144:147], v[66:69]
	global_load_dwordx4 v[116:119], v[112:113], off offset:1280
	global_load_dwordx4 v[120:123], v[112:113], off offset:1344
	global_load_dwordx4 v[124:127], v[112:113], off offset:1408
	global_load_dwordx4 v[128:131], v[112:113], off offset:1472
	global_load_dwordx4 v[132:135], v[112:113], off offset:1536
	global_load_dwordx4 v[136:139], v[112:113], off offset:1600
	global_load_dwordx4 v[140:143], v[112:113], off offset:1664
	global_load_dwordx4 v[144:147], v[112:113], off offset:1728
	ds_read_b128 v[148:151], v1 offset:512
	ds_read_b128 v[152:155], v1 offset:576
	s_waitcnt vmcnt(23) lgkmcnt(1)
	v_mfma_f32_16x16x32_bf16 v[66:69], v[148:151], v[156:159], v[66:69]
	ds_read_b128 v[188:191], v1 offset:640
	s_waitcnt vmcnt(22) lgkmcnt(1)
	v_mfma_f32_16x16x32_bf16 v[66:69], v[152:155], v[160:163], v[66:69]
	ds_read_b128 v[244:247], v1 offset:704
	s_waitcnt vmcnt(21) lgkmcnt(1)
	v_mfma_f32_16x16x32_bf16 v[66:69], v[188:191], v[164:167], v[66:69]
	ds_read_b128 v[148:151], v1 offset:768
	s_waitcnt vmcnt(20) lgkmcnt(1)
	v_mfma_f32_16x16x32_bf16 v[66:69], v[244:247], v[168:171], v[66:69]
	ds_read_b128 v[152:155], v1 offset:832
	s_waitcnt vmcnt(19) lgkmcnt(1)
	v_mfma_f32_16x16x32_bf16 v[66:69], v[148:151], v[172:175], v[66:69]
	ds_read_b128 v[188:191], v1 offset:896
	s_waitcnt vmcnt(18) lgkmcnt(1)
	v_mfma_f32_16x16x32_bf16 v[66:69], v[152:155], v[176:179], v[66:69]
	ds_read_b128 v[244:247], v1 offset:960
	s_waitcnt vmcnt(17) lgkmcnt(1)
	v_mfma_f32_16x16x32_bf16 v[66:69], v[188:191], v[180:183], v[66:69]
	s_waitcnt vmcnt(16) lgkmcnt(0)
	v_mfma_f32_16x16x32_bf16 v[66:69], v[244:247], v[184:187], v[66:69]
	ds_read_b128 v[148:151], v1 offset:1024
	ds_read_b128 v[152:155], v1 offset:1088
	s_waitcnt vmcnt(15) lgkmcnt(1)
	v_mfma_f32_16x16x32_bf16 v[66:69], v[148:151], v[208:211], v[66:69]
	ds_read_b128 v[188:191], v1 offset:1152
	s_waitcnt vmcnt(14) lgkmcnt(1)
	v_mfma_f32_16x16x32_bf16 v[66:69], v[152:155], v[212:215], v[66:69]
	ds_read_b128 v[244:247], v1 offset:1216
	s_waitcnt vmcnt(13) lgkmcnt(1)
	v_mfma_f32_16x16x32_bf16 v[66:69], v[188:191], v[216:219], v[66:69]
	ds_read_b128 v[148:151], v1 offset:1280
	s_waitcnt vmcnt(12) lgkmcnt(1)
	v_mfma_f32_16x16x32_bf16 v[66:69], v[244:247], v[220:223], v[66:69]
	ds_read_b128 v[152:155], v1 offset:1344
	s_waitcnt vmcnt(11) lgkmcnt(1)
	v_mfma_f32_16x16x32_bf16 v[66:69], v[148:151], v[224:227], v[66:69]
	ds_read_b128 v[188:191], v1 offset:1408
	s_waitcnt vmcnt(10) lgkmcnt(1)
	v_mfma_f32_16x16x32_bf16 v[66:69], v[152:155], v[228:231], v[66:69]
	ds_read_b128 v[244:247], v1 offset:1472
	s_waitcnt vmcnt(9) lgkmcnt(1)
	v_mfma_f32_16x16x32_bf16 v[66:69], v[188:191], v[232:235], v[66:69]
	s_waitcnt vmcnt(8) lgkmcnt(0)
	v_mfma_f32_16x16x32_bf16 v[66:69], v[244:247], v[236:239], v[66:69]
	ds_read_b128 v[148:151], v1 offset:1536
	ds_read_b128 v[152:155], v1 offset:1600
	s_waitcnt vmcnt(7) lgkmcnt(1)
	v_mfma_f32_16x16x32_bf16 v[66:69], v[148:151], v[116:119], v[66:69]
	ds_read_b128 v[188:191], v1 offset:1664
	s_waitcnt vmcnt(6) lgkmcnt(1)
	v_mfma_f32_16x16x32_bf16 v[66:69], v[152:155], v[120:123], v[66:69]
	ds_read_b128 v[244:247], v1 offset:1728
	s_waitcnt vmcnt(5) lgkmcnt(1)
	v_mfma_f32_16x16x32_bf16 v[66:69], v[188:191], v[124:127], v[66:69]
	ds_read_b128 v[148:151], v1 offset:1792
	s_waitcnt vmcnt(4) lgkmcnt(1)
	v_mfma_f32_16x16x32_bf16 v[66:69], v[244:247], v[128:131], v[66:69]
	ds_read_b128 v[152:155], v1 offset:1856
	s_waitcnt vmcnt(3) lgkmcnt(1)
	v_mfma_f32_16x16x32_bf16 v[66:69], v[148:151], v[132:135], v[66:69]
	ds_read_b128 v[188:191], v1 offset:1920
	s_waitcnt vmcnt(2) lgkmcnt(1)
	v_mfma_f32_16x16x32_bf16 v[66:69], v[152:155], v[136:139], v[66:69]
	ds_read_b128 v[244:247], v1 offset:1984
	s_waitcnt vmcnt(1) lgkmcnt(1)
	v_mfma_f32_16x16x32_bf16 v[66:69], v[188:191], v[140:143], v[66:69]
	s_waitcnt vmcnt(0) lgkmcnt(0)
	v_mfma_f32_16x16x32_bf16 v[66:69], v[244:247], v[144:147], v[66:69]
	s_nop 6
	ds_write2st64_b32 v200, v66, v67 offset1:1
	ds_write2st64_b32 v200, v68, v69 offset0:2 offset1:3
	s_nop 1
	s_and_b64 vcc, exec, s[56:57]
	s_cbranch_vccnz .Lp7_nopf
	s_add_i32 s16, s73, s62
	s_ashr_i32 s17, s16, 31
	s_or_b32 s18, s16, 1
	s_lshl_b64 s[20:21], s[16:17], 13
	v_readlane_b32 s76, v252, 9
	v_readlane_b32 s77, v252, 10
	s_add_u32 s20, s76, s20
	s_addc_u32 s21, s77, s21
	s_ashr_i32 s19, s18, 31
	s_lshl_b64 s[22:23], s[18:19], 13
	s_add_u32 s22, s76, s22
	s_addc_u32 s23, s77, s23
	s_lshl_b64 s[16:17], s[16:17], 12
	v_lshl_add_u64 v[66:67], v[100:101], 0, s[16:17]
	s_lshl_b64 s[16:17], s[18:19], 12
	v_lshl_add_u64 v[68:69], v[100:101], 0, s[16:17]
	global_load_dwordx4 v[2:5], v195, s[20:21]
	global_load_dwordx4 v[6:9], v195, s[20:21] offset:1024
	global_load_dwordx4 v[10:13], v195, s[22:23]
	global_load_dwordx4 v[14:17], v195, s[22:23] offset:1024
	global_load_dwordx4 v[18:21], v195, s[20:21] offset:2048
	global_load_dwordx4 v[22:25], v195, s[20:21] offset:3072
	global_load_dwordx4 v[26:29], v195, s[22:23] offset:2048
	global_load_dwordx4 v[30:33], v195, s[22:23] offset:3072
	global_load_dwordx2 v[74:75], v[66:67], off
	global_load_dwordx2 v[76:77], v[66:67], off offset:512
	global_load_dwordx2 v[78:79], v[66:67], off offset:1024
	global_load_dwordx2 v[80:81], v[66:67], off offset:1536
	global_load_dwordx2 v[82:83], v[68:69], off
	global_load_dwordx2 v[84:85], v[68:69], off offset:512
	global_load_dwordx2 v[88:89], v[68:69], off offset:1024
	global_load_dwordx2 v[90:91], v[68:69], off offset:1536
	global_load_dwordx4 v[34:37], v196, s[20:21]
	global_load_dwordx4 v[38:41], v196, s[22:23]
	global_load_dwordx4 v[42:45], v197, s[20:21]
	global_load_dwordx4 v[46:49], v197, s[22:23]
	global_load_dwordx4 v[50:53], v198, s[20:21]
	global_load_dwordx4 v[54:57], v198, s[22:23]
	global_load_dwordx4 v[58:61], v199, s[20:21]
	global_load_dwordx4 v[62:65], v199, s[22:23]
	global_load_dwordx2 v[94:95], v[66:67], off offset:2048
	global_load_dwordx2 v[96:97], v[66:67], off offset:2560
	global_load_dwordx2 v[98:99], v[66:67], off offset:3072
	global_load_dwordx2 v[102:103], v[66:67], off offset:3584
	global_load_dwordx2 v[104:105], v[68:69], off offset:2048
	global_load_dwordx2 v[106:107], v[68:69], off offset:2560
	global_load_dwordx2 v[108:109], v[68:69], off offset:3072
	global_load_dwordx2 v[110:111], v[68:69], off offset:3584
	v_readlane_b32 s78, v252, 11
	v_readlane_b32 s79, v252, 12
	v_readlane_b32 s80, v252, 13
	v_readlane_b32 s81, v252, 14
	v_readlane_b32 s82, v252, 15
	v_readlane_b32 s83, v252, 16
	v_readlane_b32 s84, v252, 17
	v_readlane_b32 s85, v252, 18
	v_readlane_b32 s86, v252, 19
	v_readlane_b32 s87, v252, 20
	v_readlane_b32 s88, v252, 21
	v_readlane_b32 s89, v252, 22
	v_readlane_b32 s90, v252, 23
	v_readlane_b32 s91, v252, 24
